# lever 4 variant: one static s_setprio 3 for the RWKV scanning waves (they share SIMDs with the polling writer waves), reset to 0 at the scan exit
# speedup vs baseline: 1.0140x; 1.0028x over previous
.LBB0_1299:
	s_or_b64 exec, exec, s[0:1]
	v_readlane_b32 s0, v232, 43
	s_ashr_i32 s15, s0, 6
	s_and_b32 s0, s15, 3
	s_waitcnt vmcnt(0)
	v_and_b32_e32 v1, 63, v70
	s_cmp_gt_u32 s0, 1
	s_waitcnt lgkmcnt(0)
	s_barrier
	s_cbranch_scc1 .Lcv0_idle
	s_and_b32 s1, s62, 2
	s_ashr_i32 s14, s96, 1
	s_or_b32 s13, s0, s1
	s_lshl_b32 s1, s0, 14
	s_and_b32 s16, s14, 1
	s_add_i32 s17, s1, 0
	s_lshl_b32 s12, s0, 6
	s_mov_b32 s18, 0
	s_mov_b64 s[6:7], -1
	s_cmp_gt_i32 s15, 3
	v_cmp_eq_u32_e64 s[0:1], 0, v1
	s_cbranch_scc1 .LBB0_1345
	s_setprio 3
	s_lshl_b32 s19, s14, 7
	s_cmp_eq_u32 s16, 0
	s_cselect_b64 s[6:7], -1, 0
	s_and_b64 s[8:9], s[6:7], exec
	s_cselect_b32 s2, 0, 0x7f
	s_cselect_b32 s3, 1, 0x7e
	s_or_b32 s22, s2, s19
	s_add_u32 s20, s4, 0x4400000
	s_addc_u32 s21, s5, 0
	s_ashr_i32 s23, s22, 31
	s_lshl_b64 s[10:11], s[22:23], 13
	s_add_u32 s24, s20, s10
	s_addc_u32 s25, s21, s11
	s_add_u32 s8, s4, 0x8400000
	s_addc_u32 s9, s5, 0
	s_add_u32 s26, s8, s10
	s_addc_u32 s27, s9, s11
	s_add_u32 s10, s4, 0x3ea00000
	v_mov_b32_e32 v175, 0
	s_addc_u32 s11, s5, 0
	s_lshl_b64 s[22:23], s[22:23], 8
	v_lshlrev_b32_e32 v54, 4, v1
	v_mov_b32_e32 v55, v175
	s_add_u32 s28, s10, s22
	v_lshlrev_b32_e32 v176, 3, v1
	v_lshl_add_u64 v[6:7], s[24:25], 0, v[54:55]
	s_movk_i32 s22, 0x1000
	v_or_b32_e32 v100, 0x800, v176
	v_add_co_u32_e32 v10, vcc, s22, v6
	v_or_b32_e32 v102, 0xc00, v176
	v_lshl_or_b32 v98, s13, 11, v176
	v_lshlrev_b32_e32 v56, 1, v100
	v_addc_co_u32_e32 v11, vcc, 0, v7, vcc
	v_lshlrev_b32_e32 v64, 1, v102
	s_addc_u32 s29, s11, s23
	v_and_b32_e32 v174, 48, v70
	global_load_dwordx4 v[38:41], v54, s[24:25]
	global_load_dwordx4 v[30:33], v54, s[24:25] offset:1024
	global_load_dwordx2 v[188:189], v98, s[26:27]
	global_load_dwordx4 v[46:49], v174, s[28:29]
	global_load_dwordx4 v[18:21], v54, s[24:25] offset:2048
	global_load_dwordx4 v[22:25], v54, s[24:25] offset:3072
	global_load_dwordx2 v[186:187], v98, s[26:27] offset:512
	global_load_dwordx4 v[42:45], v174, s[28:29] offset:64
	global_load_dwordx4 v[2:5], v56, s[24:25]
	global_load_dwordx4 v[14:17], v[10:11], off offset:1024
	global_load_dwordx2 v[182:183], v98, s[26:27] offset:1024
	global_load_dwordx4 v[26:29], v174, s[28:29] offset:128
	global_load_dwordx4 v[6:9], v64, s[24:25]
	s_nop 0
	global_load_dwordx4 v[10:13], v[10:11], off offset:3072
	s_nop 0
	global_load_dwordx2 v[184:185], v98, s[26:27] offset:1536
	global_load_dwordx4 v[34:37], v174, s[28:29] offset:192
	s_or_b32 s24, s3, s19
	s_ashr_i32 s25, s24, 31
	s_lshl_b64 s[26:27], s[24:25], 13
	s_add_u32 s28, s20, s26
	s_addc_u32 s29, s21, s27
	s_add_u32 s26, s8, s26
	s_addc_u32 s27, s9, s27
	s_lshl_b64 s[24:25], s[24:25], 8
	s_add_u32 s24, s10, s24
	v_lshl_add_u64 v[62:63], s[28:29], 0, v[54:55]
	s_addc_u32 s25, s11, s25
	global_load_dwordx4 v[78:81], v54, s[28:29]
	global_load_dwordx4 v[70:73], v54, s[28:29] offset:1024
	global_load_dwordx2 v[196:197], v98, s[26:27]
	global_load_dwordx4 v[94:97], v174, s[24:25]
	global_load_dwordx4 v[50:53], v54, s[28:29] offset:2048
	global_load_dwordx4 v[58:61], v54, s[28:29] offset:3072
	global_load_dwordx2 v[194:195], v98, s[26:27] offset:512
	global_load_dwordx4 v[82:85], v174, s[24:25] offset:64
	s_nop 0
	global_load_dwordx4 v[54:57], v56, s[28:29]
	v_add_co_u32_e32 v66, vcc, s22, v62
	v_mov_b32_e32 v99, v175
	s_nop 0
	v_addc_co_u32_e32 v67, vcc, 0, v63, vcc
	global_load_dwordx4 v[74:77], v[66:67], off offset:1024
	global_load_dwordx2 v[190:191], v98, s[26:27] offset:1024
	global_load_dwordx4 v[86:89], v174, s[24:25] offset:128
	s_nop 0
	global_load_dwordx4 v[62:65], v64, s[28:29]
	s_nop 0
	global_load_dwordx4 v[66:69], v[66:67], off offset:3072
	s_nop 0
	global_load_dwordx2 v[192:193], v98, s[26:27] offset:1536
	global_load_dwordx4 v[90:93], v174, s[24:25] offset:192
	v_lshl_add_u64 v[178:179], s[10:11], 0, v[174:175]
	v_lshl_add_u64 v[180:181], s[8:9], 0, v[98:99]
	v_add_u32_e32 v177, s17, v176
	v_lshlrev_b32_e32 v206, 1, v100
	v_lshlrev_b32_e32 v207, 1, v102
	v_mov_b32_e32 v158, v175
	v_mov_b32_e32 v159, v175
	v_mov_b32_e32 v160, v175
	v_mov_b32_e32 v161, v175
	v_mov_b32_e32 v154, v175
	v_mov_b32_e32 v155, v175
	v_mov_b32_e32 v156, v175
	v_mov_b32_e32 v157, v175
	v_mov_b32_e32 v150, v175
	v_mov_b32_e32 v151, v175
	v_mov_b32_e32 v152, v175
	v_mov_b32_e32 v153, v175
	v_mov_b32_e32 v106, v175
	v_mov_b32_e32 v107, v175
	v_mov_b32_e32 v108, v175
	v_mov_b32_e32 v109, v175

.LBB0_1356:
	s_setprio 0
	s_waitcnt lgkmcnt(0)
	s_barrier
	s_branch .LBB0_1371

.LBB0_3617:
	s_or_b64 exec, exec, s[0:1]
	s_ashr_i32 s8, s8, 6
	s_and_b32 s0, s8, 3
	s_waitcnt vmcnt(0)
	v_and_b32_e32 v1, 63, v70
	s_cmp_gt_u32 s0, 1
	s_waitcnt lgkmcnt(0)
	s_barrier
	s_cbranch_scc1 .Lcv1_idle
	s_and_b32 s1, s60, 2
	s_ashr_i32 s11, s96, 1
	s_or_b32 s10, s0, s1
	s_lshl_b32 s1, s0, 14
	s_and_b32 s18, s11, 1
	s_add_i32 s19, s1, 0
	s_lshl_b32 s9, s0, 6
	s_mov_b32 s20, 0
	s_mov_b64 s[6:7], -1
	s_cmp_gt_i32 s8, 3
	v_cmp_eq_u32_e64 s[0:1], 0, v1
	s_cbranch_scc1 .LBB0_3663
	s_setprio 3
	s_lshl_b32 s21, s11, 7
	s_cmp_eq_u32 s18, 0
	s_cselect_b64 s[6:7], -1, 0
	s_and_b64 s[2:3], s[6:7], exec
	s_cselect_b32 s2, 0, 0x7f
	s_cselect_b32 s25, 1, 0x7e
	s_or_b32 s2, s2, s21
	s_add_u32 s22, s4, 0x4400000
	s_addc_u32 s23, s5, 0
	s_ashr_i32 s3, s2, 31
	s_lshl_b64 s[14:15], s[2:3], 13
	s_add_u32 s16, s22, s14
	s_addc_u32 s17, s23, s15
	s_add_u32 s12, s4, 0x8400000
	s_addc_u32 s13, s5, 0
	s_add_u32 s26, s12, s14
	v_mov_b32_e32 v187, 0
	s_addc_u32 s27, s13, s15
	v_lshlrev_b32_e32 v14, 4, v1
	v_mov_b32_e32 v15, v187
	s_add_u32 s14, s4, 0x3ea00000
	v_lshl_add_u64 v[2:3], s[16:17], 0, v[14:15]
	s_movk_i32 s24, 0x1000
	s_addc_u32 s15, s5, 0
	s_lshl_b64 s[2:3], s[2:3], 8
	v_add_co_u32_e32 v2, vcc, s24, v2
	s_add_u32 s2, s14, s2
	v_lshlrev_b32_e32 v188, 3, v1
	v_addc_co_u32_e32 v3, vcc, 0, v3, vcc
	s_addc_u32 s3, s15, s3
	v_and_b32_e32 v186, 48, v70
	global_load_dwordx4 v[42:45], v14, s[16:17]
	global_load_dwordx4 v[34:37], v14, s[16:17] offset:1024
	v_lshl_or_b32 v98, s10, 11, v188
	global_load_dwordx4 v[18:21], v14, s[16:17] offset:2048
	global_load_dwordx4 v[22:25], v14, s[16:17] offset:3072
	global_load_dwordx4 v[46:49], v186, s[2:3]
	global_load_dwordx4 v[26:29], v186, s[2:3] offset:64
	global_load_dwordx4 v[10:13], v[2:3], off offset:1024
	s_nop 0
	global_load_dwordx4 v[2:5], v[2:3], off offset:3072
	s_nop 0
	global_load_dwordx2 v[196:197], v98, s[26:27]
	global_load_dwordx2 v[184:185], v98, s[26:27] offset:512
	global_load_dwordx2 v[182:183], v98, s[26:27] offset:1024
	global_load_dwordx2 v[194:195], v98, s[26:27] offset:1536
	global_load_dwordx4 v[30:33], v186, s[2:3] offset:128
	global_load_dwordx4 v[6:9], v186, s[2:3] offset:192
	s_or_b32 s2, s25, s21
	s_ashr_i32 s3, s2, 31
	s_lshl_b64 s[26:27], s[2:3], 13
	s_add_u32 s28, s22, s26
	s_addc_u32 s29, s23, s27
	s_add_u32 s26, s12, s26
	v_or_b32_e32 v100, 0x800, v188
	s_addc_u32 s27, s13, s27
	s_lshl_b64 s[2:3], s[2:3], 8
	v_lshlrev_b32_e32 v50, 1, v100
	s_add_u32 s2, s14, s2
	v_lshl_add_u64 v[16:17], s[28:29], 0, v[14:15]
	v_or_b32_e32 v102, 0xc00, v188
	s_addc_u32 s3, s15, s3
	global_load_dwordx4 v[86:89], v14, s[28:29]
	global_load_dwordx4 v[78:81], v14, s[28:29] offset:1024
	global_load_dwordx4 v[62:65], v14, s[28:29] offset:2048
	global_load_dwordx4 v[66:69], v14, s[28:29] offset:3072
	global_load_dwordx4 v[94:97], v186, s[2:3]
	global_load_dwordx4 v[82:85], v186, s[2:3] offset:64
	global_load_dwordx4 v[38:41], v50, s[16:17]
	global_load_dwordx4 v[58:61], v50, s[28:29]
	v_add_co_u32_e32 v50, vcc, s24, v16
	v_lshlrev_b32_e32 v52, 1, v102
	s_nop 0
	v_addc_co_u32_e32 v51, vcc, 0, v17, vcc
	global_load_dwordx4 v[14:17], v52, s[16:17]
	global_load_dwordx4 v[54:57], v52, s[28:29]
	global_load_dwordx4 v[70:73], v[50:51], off offset:1024
	s_nop 0
	global_load_dwordx4 v[50:53], v[50:51], off offset:3072
	s_nop 0
	global_load_dwordx2 v[204:205], v98, s[26:27]
	global_load_dwordx2 v[202:203], v98, s[26:27] offset:512
	global_load_dwordx2 v[200:201], v98, s[26:27] offset:1024
	global_load_dwordx2 v[198:199], v98, s[26:27] offset:1536
	global_load_dwordx4 v[90:93], v186, s[2:3] offset:128
	global_load_dwordx4 v[74:77], v186, s[2:3] offset:192
	v_mov_b32_e32 v99, v187
	v_lshl_add_u64 v[190:191], s[14:15], 0, v[186:187]
	v_lshl_add_u64 v[192:193], s[12:13], 0, v[98:99]
	v_add_u32_e32 v189, s19, v188
	v_lshlrev_b32_e32 v220, 1, v100
	v_lshlrev_b32_e32 v221, 1, v102
	v_mov_b32_e32 v154, v187
	v_mov_b32_e32 v155, v187
	v_mov_b32_e32 v156, v187
	v_mov_b32_e32 v157, v187
	v_mov_b32_e32 v150, v187
	v_mov_b32_e32 v151, v187
	v_mov_b32_e32 v152, v187
	v_mov_b32_e32 v153, v187
	v_mov_b32_e32 v102, v187
	v_mov_b32_e32 v103, v187
	v_mov_b32_e32 v104, v187
	v_mov_b32_e32 v105, v187
	v_mov_b32_e32 v106, v187
	v_mov_b32_e32 v107, v187
	v_mov_b32_e32 v108, v187
	v_mov_b32_e32 v109, v187
